# epilogue de-serialisation: w_o projection epilogue issues all 16 residual loads up front into free fragment registers instead of 8 dependent load rounds (plus rotary table loads four at a time)
# speedup vs baseline: 1.0026x; 1.0026x over previous
; DI unsigned cvt_pk_bf16(float lo, float hi) { const f32x2_t v = {lo, hi}; return __builtin_bit_cast(unsigned, __builtin_convertvector(v, bf16x2_t)); }
;     DI void operator()(const f32x4 (&acc)[2][2][4][2], const Unit& u, int wr, int wc, int fr, int fq) const {
;     ...
;             for (int m = 0; m < 4; ++m) { const size_t r = (size_t)(row0 + ai * HALF + m * 16);
; #pragma unroll
;                 for (int bj = 0; bj < 2; ++bj) { const size_t o = r * D_ + col0 + bj * HALF; f32x4 x0, x1; unpack8f(*(const u32x4*)(R0 + o), x0, x1);
;                     f32x4 v0 = ALPHA * x0 + acc[ai][bj][m][0], v1 = ALPHA * x1 + acc[ai][bj][m][1];
;                     if (HAS_R1) { f32x4 q0, q1; unpack8f(*(const u32x4*)(R1 + o), q0, q1); v0 = v0 + q0; v1 = v1 + q1; }
;                     u32x4 w; w.x = cvt_pk_bf16(v0[0], v0[1]); w.y = cvt_pk_bf16(v0[2], v0[3]); w.z = cvt_pk_bf16(v1[0], v1[1]); w.w = cvt_pk_bf16(v1[2], v1[3]);
;                     *(u32x4*)(Yo + o) = w; }
;                 if (m & 1) asm volatile("" ::: "memory"); }
;     }
.LBB0_572:
	v_lshl_add_u32 v166, s62, 8, v138
	v_lshl_or_b32 v168, s92, 8, v139
	v_ashrrev_i32_e32 v167, 31, v166
	v_ashrrev_i32_e32 v169, 31, v168
	v_lshlrev_b64 v[170:171], 11, v[166:167]
	v_lshl_add_u64 v[172:173], v[170:171], 0, v[168:169]
	v_lshlrev_b64 v[174:175], 1, v[172:173]
	v_lshl_add_u64 v[176:177], s[10:11], 0, v[174:175]
	global_load_dwordx4 v[248:251], v[176:177], off
	v_or_b32_e32 v176, 0x100, v174
	v_mov_b32_e32 v177, v175
	v_lshl_add_u64 v[178:179], s[10:11], 0, v[176:177]
	global_load_dwordx4 v[244:247], v[178:179], off
	v_lshl_add_u64 v[176:177], v[174:175], 0, s[18:19]
	v_lshl_add_u64 v[178:179], s[10:11], 0, v[176:177]
	global_load_dwordx4 v[240:243], v[178:179], off
	v_lshl_add_u64 v[176:177], v[174:175], 0, s[20:21]
	v_lshl_add_u64 v[178:179], s[10:11], 0, v[176:177]
	global_load_dwordx4 v[236:239], v[178:179], off
	v_lshl_add_u64 v[176:177], v[174:175], 0, s[22:23]
	v_lshl_add_u64 v[178:179], s[10:11], 0, v[176:177]
	global_load_dwordx4 v[232:235], v[178:179], off
	v_lshl_add_u64 v[176:177], v[174:175], 0, s[24:25]
	v_lshl_add_u64 v[178:179], s[10:11], 0, v[176:177]
	global_load_dwordx4 v[228:231], v[178:179], off
	v_lshl_add_u64 v[176:177], v[174:175], 0, s[26:27]
	v_lshl_add_u64 v[178:179], s[10:11], 0, v[176:177]
	global_load_dwordx4 v[224:227], v[178:179], off
	v_lshl_add_u64 v[176:177], v[174:175], 0, s[28:29]
	v_lshl_add_u64 v[178:179], s[10:11], 0, v[176:177]
	global_load_dwordx4 v[220:223], v[178:179], off
	s_mov_b64 s[64:65], 0x80000
	v_lshl_add_u64 v[176:177], v[174:175], 0, s[64:65]
	v_lshl_add_u64 v[178:179], s[10:11], 0, v[176:177]
	global_load_dwordx4 v[216:219], v[178:179], off
	v_lshl_add_u64 v[176:177], v[174:175], 0, s[40:41]
	v_lshl_add_u64 v[178:179], s[10:11], 0, v[176:177]
	global_load_dwordx4 v[212:215], v[178:179], off
	v_lshl_add_u64 v[176:177], v[174:175], 0, s[42:43]
	v_lshl_add_u64 v[178:179], s[10:11], 0, v[176:177]
	global_load_dwordx4 v[208:211], v[178:179], off
	v_lshl_add_u64 v[176:177], v[174:175], 0, s[44:45]
	v_lshl_add_u64 v[178:179], s[10:11], 0, v[176:177]
	global_load_dwordx4 v[204:207], v[178:179], off
	v_lshl_add_u64 v[176:177], v[174:175], 0, s[46:47]
	v_lshl_add_u64 v[178:179], s[10:11], 0, v[176:177]
	global_load_dwordx4 v[200:203], v[178:179], off
	v_lshl_add_u64 v[176:177], v[174:175], 0, s[48:49]
	v_lshl_add_u64 v[178:179], s[10:11], 0, v[176:177]
	global_load_dwordx4 v[196:199], v[178:179], off
	v_lshl_add_u64 v[176:177], v[174:175], 0, s[50:51]
	v_lshl_add_u64 v[178:179], s[10:11], 0, v[176:177]
	global_load_dwordx4 v[192:195], v[178:179], off
	v_lshl_add_u64 v[176:177], v[174:175], 0, s[52:53]
	v_lshl_add_u64 v[178:179], s[10:11], 0, v[176:177]
	global_load_dwordx4 v[188:191], v[178:179], off
	v_lshl_add_u32 v132, s62, 8, v138
	v_lshl_or_b32 v146, s92, 8, v139
	v_ashrrev_i32_e32 v133, 31, v132
	v_ashrrev_i32_e32 v147, 31, v146
	v_lshlrev_b64 v[132:133], 11, v[132:133]
	v_lshl_add_u64 v[132:133], v[132:133], 0, v[146:147]
	v_lshlrev_b64 v[132:133], 1, v[132:133]
	v_lshl_add_u64 v[146:147], s[10:11], 0, v[132:133]
	v_or_b32_e32 v154, 0x100, v132
	v_mov_b32_e32 v155, v133
	s_nop 0
	v_lshl_add_u64 v[150:151], s[10:11], 0, v[154:155]
	s_nop 0
	v_lshl_add_u64 v[156:157], s[12:13], 0, v[132:133]
	v_lshl_add_u64 v[158:159], v[132:133], 0, s[18:19]
	v_lshl_add_u64 v[154:155], s[12:13], 0, v[154:155]
	v_lshl_add_u64 v[160:161], s[10:11], 0, v[158:159]
	s_andn2_b64 vcc, exec, s[4:5]
	s_mov_b64 s[4:5], -1
	s_nop 0
	s_waitcnt vmcnt(15)
	v_lshlrev_b32_e32 v162, 16, v248
	v_and_b32_e32 v163, 0xffff0000, v248
	v_lshlrev_b32_e32 v146, 16, v249
	v_and_b32_e32 v147, 0xffff0000, v249
	v_lshlrev_b32_e32 v164, 16, v250
	v_and_b32_e32 v165, 0xffff0000, v250
	v_lshlrev_b32_e32 v148, 16, v251
	v_and_b32_e32 v149, 0xffff0000, v251
	v_pk_fma_f32 v[126:127], v[146:147], s[16:17], v[126:127] op_sel_hi:[1,0,1]
	v_pk_fma_f32 v[124:125], v[162:163], s[16:17], v[124:125] op_sel_hi:[1,0,1]
	v_pk_fma_f32 v[146:147], v[148:149], s[16:17], v[122:123] op_sel_hi:[1,0,1]
	s_nop 0
	s_waitcnt vmcnt(14)
	v_lshlrev_b32_e32 v148, 16, v244
	v_and_b32_e32 v149, 0xffff0000, v244
	v_lshlrev_b32_e32 v150, 16, v245
	v_and_b32_e32 v151, 0xffff0000, v245
	v_lshlrev_b32_e32 v162, 16, v246
	v_and_b32_e32 v163, 0xffff0000, v246
	v_lshlrev_b32_e32 v152, 16, v247
	v_and_b32_e32 v153, 0xffff0000, v247
	v_pk_fma_f32 v[122:123], v[164:165], s[16:17], v[120:121] op_sel_hi:[1,0,1]
	v_cvt_pk_bf16_f32 v120, v124, v125
	v_pk_fma_f32 v[118:119], v[150:151], s[16:17], v[118:119] op_sel_hi:[1,0,1]
	v_pk_fma_f32 v[116:117], v[148:149], s[16:17], v[116:117] op_sel_hi:[1,0,1]
	v_pk_fma_f32 v[124:125], v[152:153], s[16:17], v[114:115] op_sel_hi:[1,0,1]
	v_pk_fma_f32 v[114:115], v[162:163], s[16:17], v[112:113] op_sel_hi:[1,0,1]
	v_cvt_pk_bf16_f32 v121, v126, v127
	v_cvt_pk_bf16_f32 v122, v122, v123
	v_cvt_pk_bf16_f32 v123, v146, v147
	v_cvt_pk_bf16_f32 v112, v116, v117
	v_cvt_pk_bf16_f32 v113, v118, v119
	v_cvt_pk_bf16_f32 v114, v114, v115
	v_cvt_pk_bf16_f32 v115, v124, v125
	global_store_dwordx4 v[156:157], v[120:123], off
	global_store_dwordx4 v[154:155], v[112:115], off
	s_nop 0
	v_lshl_add_u64 v[120:121], v[132:133], 0, s[20:21]
	v_lshl_add_u64 v[116:117], s[10:11], 0, v[120:121]
	s_nop 0
	v_lshl_add_u64 v[124:125], s[12:13], 0, v[158:159]
	v_lshl_add_u64 v[122:123], v[132:133], 0, s[22:23]
	v_lshl_add_u64 v[120:121], s[12:13], 0, v[120:121]
	v_lshl_add_u64 v[126:127], s[10:11], 0, v[122:123]
	s_nop 0
	s_waitcnt vmcnt(15)
	v_lshlrev_b32_e32 v146, 16, v240
	v_and_b32_e32 v147, 0xffff0000, v240
	v_lshlrev_b32_e32 v112, 16, v241
	v_and_b32_e32 v113, 0xffff0000, v241
	v_lshlrev_b32_e32 v148, 16, v242
	v_and_b32_e32 v149, 0xffff0000, v242
	v_lshlrev_b32_e32 v114, 16, v243
	v_and_b32_e32 v115, 0xffff0000, v243
	s_nop 0
	s_waitcnt vmcnt(14)
; DI unsigned cvt_pk_bf16(float lo, float hi) { const f32x2_t v = {lo, hi}; return __builtin_bit_cast(unsigned, __builtin_convertvector(v, bf16x2_t)); }
;     DI void operator()(const f32x4 (&acc)[2][2][4][2], const Unit& u, int wr, int wc, int fr, int fq) const {
;     ...
;             for (int m = 0; m < 4; ++m) { const size_t r = (size_t)(row0 + ai * HALF + m * 16);
; #pragma unroll
;                 for (int bj = 0; bj < 2; ++bj) { const size_t o = r * D_ + col0 + bj * HALF; f32x4 x0, x1; unpack8f(*(const u32x4*)(R0 + o), x0, x1);
;                     f32x4 v0 = ALPHA * x0 + acc[ai][bj][m][0], v1 = ALPHA * x1 + acc[ai][bj][m][1];
;                     if (HAS_R1) { f32x4 q0, q1; unpack8f(*(const u32x4*)(R1 + o), q0, q1); v0 = v0 + q0; v1 = v1 + q1; }
;                     u32x4 w; w.x = cvt_pk_bf16(v0[0], v0[1]); w.y = cvt_pk_bf16(v0[2], v0[3]); w.z = cvt_pk_bf16(v1[0], v1[1]); w.w = cvt_pk_bf16(v1[2], v1[3]);
;                     *(u32x4*)(Yo + o) = w; }
;                 if (m & 1) asm volatile("" ::: "memory"); }
;     }
	v_lshlrev_b32_e32 v150, 16, v236
	v_and_b32_e32 v151, 0xffff0000, v236
	v_lshlrev_b32_e32 v116, 16, v237
	v_and_b32_e32 v117, 0xffff0000, v237
	v_lshlrev_b32_e32 v152, 16, v238
	v_and_b32_e32 v153, 0xffff0000, v238
	v_lshlrev_b32_e32 v118, 16, v239
	v_and_b32_e32 v119, 0xffff0000, v239
	v_pk_fma_f32 v[110:111], v[112:113], s[16:17], v[110:111] op_sel_hi:[1,0,1]
	v_pk_fma_f32 v[108:109], v[146:147], s[16:17], v[108:109] op_sel_hi:[1,0,1]
	v_pk_fma_f32 v[106:107], v[114:115], s[16:17], v[106:107] op_sel_hi:[1,0,1]
	v_pk_fma_f32 v[104:105], v[148:149], s[16:17], v[104:105] op_sel_hi:[1,0,1]
	v_pk_fma_f32 v[102:103], v[116:117], s[16:17], v[102:103] op_sel_hi:[1,0,1]
	v_pk_fma_f32 v[100:101], v[150:151], s[16:17], v[100:101] op_sel_hi:[1,0,1]
	v_pk_fma_f32 v[112:113], v[118:119], s[16:17], v[98:99] op_sel_hi:[1,0,1]
	v_pk_fma_f32 v[114:115], v[152:153], s[16:17], v[96:97] op_sel_hi:[1,0,1]
	v_cvt_pk_bf16_f32 v96, v108, v109
	v_cvt_pk_bf16_f32 v97, v110, v111
	v_cvt_pk_bf16_f32 v98, v104, v105
	v_cvt_pk_bf16_f32 v99, v106, v107
	v_cvt_pk_bf16_f32 v100, v100, v101
	v_cvt_pk_bf16_f32 v101, v102, v103
	v_cvt_pk_bf16_f32 v102, v114, v115
	v_cvt_pk_bf16_f32 v103, v112, v113
	global_store_dwordx4 v[124:125], v[96:99], off
	global_store_dwordx4 v[120:121], v[100:103], off
	v_lshl_add_u64 v[104:105], v[132:133], 0, s[24:25]
	s_nop 0
	v_lshl_add_u64 v[100:101], s[10:11], 0, v[104:105]
	s_nop 0
	v_lshl_add_u64 v[106:107], v[132:133], 0, s[26:27]
	v_lshl_add_u64 v[108:109], s[12:13], 0, v[122:123]
	v_lshl_add_u64 v[104:105], s[12:13], 0, v[104:105]
	v_lshl_add_u64 v[110:111], s[10:11], 0, v[106:107]
	s_nop 0
	s_waitcnt vmcnt(15)
	v_lshlrev_b32_e32 v112, 16, v232
	v_and_b32_e32 v113, 0xffff0000, v232
	v_lshlrev_b32_e32 v96, 16, v233
	v_and_b32_e32 v97, 0xffff0000, v233
	v_lshlrev_b32_e32 v114, 16, v234
	v_and_b32_e32 v115, 0xffff0000, v234
	v_lshlrev_b32_e32 v98, 16, v235
	v_and_b32_e32 v99, 0xffff0000, v235
	s_nop 0
	s_waitcnt vmcnt(14)
	v_lshlrev_b32_e32 v116, 16, v228
	v_and_b32_e32 v117, 0xffff0000, v228
	v_lshlrev_b32_e32 v100, 16, v229
	v_and_b32_e32 v101, 0xffff0000, v229
	v_lshlrev_b32_e32 v118, 16, v230
	v_and_b32_e32 v119, 0xffff0000, v230
	v_lshlrev_b32_e32 v102, 16, v231
	v_and_b32_e32 v103, 0xffff0000, v231
	v_pk_fma_f32 v[94:95], v[96:97], s[16:17], v[94:95] op_sel_hi:[1,0,1]
	v_pk_fma_f32 v[92:93], v[112:113], s[16:17], v[92:93] op_sel_hi:[1,0,1]
	v_pk_fma_f32 v[90:91], v[98:99], s[16:17], v[90:91] op_sel_hi:[1,0,1]
	v_pk_fma_f32 v[88:89], v[114:115], s[16:17], v[88:89] op_sel_hi:[1,0,1]
	v_pk_fma_f32 v[86:87], v[100:101], s[16:17], v[86:87] op_sel_hi:[1,0,1]
	v_pk_fma_f32 v[84:85], v[116:117], s[16:17], v[84:85] op_sel_hi:[1,0,1]
	v_pk_fma_f32 v[96:97], v[102:103], s[16:17], v[82:83] op_sel_hi:[1,0,1]
	v_pk_fma_f32 v[98:99], v[118:119], s[16:17], v[80:81] op_sel_hi:[1,0,1]
	v_cvt_pk_bf16_f32 v80, v92, v93
	v_cvt_pk_bf16_f32 v81, v94, v95
	v_cvt_pk_bf16_f32 v82, v88, v89
	v_cvt_pk_bf16_f32 v83, v90, v91
	v_cvt_pk_bf16_f32 v84, v84, v85
	v_cvt_pk_bf16_f32 v85, v86, v87
	v_cvt_pk_bf16_f32 v86, v98, v99
	v_cvt_pk_bf16_f32 v87, v96, v97
	global_store_dwordx4 v[108:109], v[80:83], off
	global_store_dwordx4 v[104:105], v[84:87], off
	v_lshl_add_u64 v[88:89], v[132:133], 0, s[28:29]
	s_nop 0
	v_lshl_add_u64 v[84:85], s[10:11], 0, v[88:89]
	s_nop 0
	v_lshl_add_u64 v[92:93], s[12:13], 0, v[106:107]
	v_lshl_add_u64 v[90:91], v[132:133], 0, s[64:65]
	v_lshl_add_u64 v[88:89], s[12:13], 0, v[88:89]
	v_lshl_add_u64 v[94:95], s[10:11], 0, v[90:91]
	s_nop 0
	s_waitcnt vmcnt(15)
	v_lshlrev_b32_e32 v96, 16, v224
	v_and_b32_e32 v97, 0xffff0000, v224
	v_lshlrev_b32_e32 v80, 16, v225
	v_and_b32_e32 v81, 0xffff0000, v225
	v_lshlrev_b32_e32 v98, 16, v226
	v_and_b32_e32 v99, 0xffff0000, v226
	v_lshlrev_b32_e32 v82, 16, v227
	v_and_b32_e32 v83, 0xffff0000, v227
	s_nop 0
	s_waitcnt vmcnt(14)
	v_lshlrev_b32_e32 v100, 16, v220
	v_and_b32_e32 v101, 0xffff0000, v220
	v_lshlrev_b32_e32 v84, 16, v221
	v_and_b32_e32 v85, 0xffff0000, v221
	v_lshlrev_b32_e32 v102, 16, v222
	v_and_b32_e32 v103, 0xffff0000, v222
	v_lshlrev_b32_e32 v86, 16, v223
	v_and_b32_e32 v87, 0xffff0000, v223
	v_pk_fma_f32 v[78:79], v[80:81], s[16:17], v[78:79] op_sel_hi:[1,0,1]
	v_pk_fma_f32 v[76:77], v[96:97], s[16:17], v[76:77] op_sel_hi:[1,0,1]
	v_pk_fma_f32 v[74:75], v[82:83], s[16:17], v[74:75] op_sel_hi:[1,0,1]
	v_pk_fma_f32 v[72:73], v[98:99], s[16:17], v[72:73] op_sel_hi:[1,0,1]
	v_pk_fma_f32 v[70:71], v[84:85], s[16:17], v[70:71] op_sel_hi:[1,0,1]
	v_pk_fma_f32 v[68:69], v[100:101], s[16:17], v[68:69] op_sel_hi:[1,0,1]
	v_pk_fma_f32 v[80:81], v[86:87], s[16:17], v[66:67] op_sel_hi:[1,0,1]
	v_pk_fma_f32 v[82:83], v[102:103], s[16:17], v[64:65] op_sel_hi:[1,0,1]
	v_cvt_pk_bf16_f32 v64, v76, v77
	v_cvt_pk_bf16_f32 v65, v78, v79
	v_cvt_pk_bf16_f32 v66, v72, v73
	v_cvt_pk_bf16_f32 v67, v74, v75
	v_cvt_pk_bf16_f32 v68, v68, v69
	v_cvt_pk_bf16_f32 v69, v70, v71
	v_cvt_pk_bf16_f32 v70, v82, v83
	v_cvt_pk_bf16_f32 v71, v80, v81
	global_store_dwordx4 v[92:93], v[64:67], off
	global_store_dwordx4 v[88:89], v[68:71], off
	v_lshl_add_u64 v[72:73], v[132:133], 0, s[40:41]
	s_nop 0
	v_lshl_add_u64 v[68:69], s[10:11], 0, v[72:73]
	s_nop 0
	v_lshl_add_u64 v[74:75], v[132:133], 0, s[42:43]
	v_lshl_add_u64 v[76:77], s[12:13], 0, v[90:91]
	v_lshl_add_u64 v[72:73], s[12:13], 0, v[72:73]
	v_lshl_add_u64 v[78:79], s[10:11], 0, v[74:75]
	s_nop 0
	s_waitcnt vmcnt(15)
	v_lshlrev_b32_e32 v80, 16, v216
	v_and_b32_e32 v81, 0xffff0000, v216
	v_lshlrev_b32_e32 v64, 16, v217
	v_and_b32_e32 v65, 0xffff0000, v217
	v_lshlrev_b32_e32 v82, 16, v218
	v_and_b32_e32 v83, 0xffff0000, v218
	v_lshlrev_b32_e32 v66, 16, v219
	v_and_b32_e32 v67, 0xffff0000, v219
	s_nop 0
	s_waitcnt vmcnt(14)
; DI unsigned cvt_pk_bf16(float lo, float hi) { const f32x2_t v = {lo, hi}; return __builtin_bit_cast(unsigned, __builtin_convertvector(v, bf16x2_t)); }
; #define PG8_BAR __builtin_amdgcn_s_barrier()
;     DI int nt(const Unit& u) const { return (u.aux & 8) ? PLED / 64 : ((u.aux & 4) ? (D_ / 2) / 64 : D_ / 64); }
; template <class Epi, class Sched, bool ALIGN_EPI, bool FP8 = false>
; DI void gemm_phase(LAS unsigned char* lds, const Gemm g, const Sched& S, const Epi& E) {
;     ...
;         if (!has_next) break;
; #pragma unroll
;         for (int a = 0; a < 2; ++a)
; #pragma unroll
;             for (int b = 0; b < 2; ++b)
; #pragma unroll
;                 for (int m = 0; m < 4; ++m)
; #pragma unroll
;                     for (int n = 0; n < 2; ++n) acc[a][b][m][n] = (f32x4){0.f, 0.f, 0.f, 0.f};
;         cur = nxt; cA = nA; cB = nB; ++ui;
;         if constexpr (sched_vark<Sched>::value) nt = S.nt(cur);
;         if constexpr (ALIGN_EPI) { if (wr == 1) PG8_BAR; }
;     DI void operator()(const f32x4 (&acc)[2][2][4][2], const Unit& u, int wr, int wc, int fr, int fq) const {
;     ...
;             for (int m = 0; m < 4; ++m) { const size_t r = (size_t)(row0 + ai * HALF + m * 16);
; #pragma unroll
;                 for (int bj = 0; bj < 2; ++bj) { const size_t o = r * D_ + col0 + bj * HALF; f32x4 x0, x1; unpack8f(*(const u32x4*)(R0 + o), x0, x1);
;                     f32x4 v0 = ALPHA * x0 + acc[ai][bj][m][0], v1 = ALPHA * x1 + acc[ai][bj][m][1];
;                     if (HAS_R1) { f32x4 q0, q1; unpack8f(*(const u32x4*)(R1 + o), q0, q1); v0 = v0 + q0; v1 = v1 + q1; }
;                     u32x4 w; w.x = cvt_pk_bf16(v0[0], v0[1]); w.y = cvt_pk_bf16(v0[2], v0[3]); w.z = cvt_pk_bf16(v1[0], v1[1]); w.w = cvt_pk_bf16(v1[2], v1[3]);
;                     *(u32x4*)(Yo + o) = w; }
;                 if (m & 1) asm volatile("" ::: "memory"); }
;     }
	v_lshlrev_b32_e32 v84, 16, v212
	v_and_b32_e32 v85, 0xffff0000, v212
	v_lshlrev_b32_e32 v68, 16, v213
	v_and_b32_e32 v69, 0xffff0000, v213
	v_lshlrev_b32_e32 v86, 16, v214
	v_and_b32_e32 v87, 0xffff0000, v214
	v_lshlrev_b32_e32 v70, 16, v215
	v_and_b32_e32 v71, 0xffff0000, v215
	v_pk_fma_f32 v[62:63], v[64:65], s[16:17], v[62:63] op_sel_hi:[1,0,1]
	v_pk_fma_f32 v[60:61], v[80:81], s[16:17], v[60:61] op_sel_hi:[1,0,1]
	v_pk_fma_f32 v[58:59], v[66:67], s[16:17], v[58:59] op_sel_hi:[1,0,1]
	v_pk_fma_f32 v[56:57], v[82:83], s[16:17], v[56:57] op_sel_hi:[1,0,1]
	v_pk_fma_f32 v[54:55], v[68:69], s[16:17], v[54:55] op_sel_hi:[1,0,1]
	v_pk_fma_f32 v[52:53], v[84:85], s[16:17], v[52:53] op_sel_hi:[1,0,1]
	v_pk_fma_f32 v[64:65], v[70:71], s[16:17], v[50:51] op_sel_hi:[1,0,1]
	v_pk_fma_f32 v[66:67], v[86:87], s[16:17], v[48:49] op_sel_hi:[1,0,1]
	v_cvt_pk_bf16_f32 v48, v60, v61
	v_cvt_pk_bf16_f32 v49, v62, v63
	v_cvt_pk_bf16_f32 v50, v56, v57
	v_cvt_pk_bf16_f32 v51, v58, v59
	v_cvt_pk_bf16_f32 v52, v52, v53
	v_cvt_pk_bf16_f32 v53, v54, v55
	v_cvt_pk_bf16_f32 v54, v66, v67
	v_cvt_pk_bf16_f32 v55, v64, v65
	global_store_dwordx4 v[76:77], v[48:51], off
	global_store_dwordx4 v[72:73], v[52:55], off
	v_lshl_add_u64 v[56:57], v[132:133], 0, s[44:45]
	s_nop 0
	v_lshl_add_u64 v[52:53], s[10:11], 0, v[56:57]
	s_nop 0
	v_lshl_add_u64 v[60:61], s[12:13], 0, v[74:75]
	v_lshl_add_u64 v[58:59], v[132:133], 0, s[46:47]
	v_lshl_add_u64 v[56:57], s[12:13], 0, v[56:57]
	v_lshl_add_u64 v[62:63], s[10:11], 0, v[58:59]
	s_nop 0
	s_waitcnt vmcnt(15)
	v_lshlrev_b32_e32 v64, 16, v208
	v_and_b32_e32 v65, 0xffff0000, v208
	v_lshlrev_b32_e32 v48, 16, v209
	v_and_b32_e32 v49, 0xffff0000, v209
	v_lshlrev_b32_e32 v66, 16, v210
	v_and_b32_e32 v67, 0xffff0000, v210
	v_lshlrev_b32_e32 v50, 16, v211
	v_and_b32_e32 v51, 0xffff0000, v211
	s_nop 0
	s_waitcnt vmcnt(14)
	v_lshlrev_b32_e32 v68, 16, v204
	v_and_b32_e32 v69, 0xffff0000, v204
	v_lshlrev_b32_e32 v52, 16, v205
	v_and_b32_e32 v53, 0xffff0000, v205
	v_lshlrev_b32_e32 v70, 16, v206
	v_and_b32_e32 v71, 0xffff0000, v206
	v_lshlrev_b32_e32 v54, 16, v207
	v_and_b32_e32 v55, 0xffff0000, v207
	v_pk_fma_f32 v[46:47], v[48:49], s[16:17], v[46:47] op_sel_hi:[1,0,1]
	v_pk_fma_f32 v[44:45], v[64:65], s[16:17], v[44:45] op_sel_hi:[1,0,1]
	v_pk_fma_f32 v[42:43], v[50:51], s[16:17], v[42:43] op_sel_hi:[1,0,1]
	v_pk_fma_f32 v[40:41], v[66:67], s[16:17], v[40:41] op_sel_hi:[1,0,1]
	v_pk_fma_f32 v[38:39], v[52:53], s[16:17], v[38:39] op_sel_hi:[1,0,1]
	v_pk_fma_f32 v[36:37], v[68:69], s[16:17], v[36:37] op_sel_hi:[1,0,1]
	v_pk_fma_f32 v[48:49], v[54:55], s[16:17], v[34:35] op_sel_hi:[1,0,1]
	v_pk_fma_f32 v[50:51], v[70:71], s[16:17], v[32:33] op_sel_hi:[1,0,1]
	v_cvt_pk_bf16_f32 v32, v44, v45
	v_cvt_pk_bf16_f32 v33, v46, v47
	v_cvt_pk_bf16_f32 v34, v40, v41
	v_cvt_pk_bf16_f32 v35, v42, v43
	v_cvt_pk_bf16_f32 v36, v36, v37
	v_cvt_pk_bf16_f32 v37, v38, v39
	v_cvt_pk_bf16_f32 v38, v50, v51
	v_cvt_pk_bf16_f32 v39, v48, v49
	global_store_dwordx4 v[60:61], v[32:35], off
	global_store_dwordx4 v[56:57], v[36:39], off
	v_lshl_add_u64 v[40:41], v[132:133], 0, s[48:49]
	s_nop 0
	v_lshl_add_u64 v[36:37], s[10:11], 0, v[40:41]
	s_nop 0
	v_lshl_add_u64 v[42:43], v[132:133], 0, s[50:51]
	v_lshl_add_u64 v[44:45], s[12:13], 0, v[58:59]
	v_lshl_add_u64 v[40:41], s[12:13], 0, v[40:41]
	v_lshl_add_u64 v[46:47], s[10:11], 0, v[42:43]
	s_nop 0
	s_waitcnt vmcnt(15)
	v_lshlrev_b32_e32 v48, 16, v200
	v_and_b32_e32 v49, 0xffff0000, v200
	v_lshlrev_b32_e32 v32, 16, v201
	v_and_b32_e32 v33, 0xffff0000, v201
	v_lshlrev_b32_e32 v50, 16, v202
	v_and_b32_e32 v51, 0xffff0000, v202
	v_lshlrev_b32_e32 v34, 16, v203
	v_and_b32_e32 v35, 0xffff0000, v203
	s_nop 0
	s_waitcnt vmcnt(14)
	v_lshlrev_b32_e32 v52, 16, v196
	v_and_b32_e32 v53, 0xffff0000, v196
	v_lshlrev_b32_e32 v36, 16, v197
	v_and_b32_e32 v37, 0xffff0000, v197
	v_lshlrev_b32_e32 v54, 16, v198
	v_and_b32_e32 v55, 0xffff0000, v198
	v_lshlrev_b32_e32 v38, 16, v199
	v_and_b32_e32 v39, 0xffff0000, v199
	v_pk_fma_f32 v[30:31], v[32:33], s[16:17], v[30:31] op_sel_hi:[1,0,1]
	v_pk_fma_f32 v[28:29], v[48:49], s[16:17], v[28:29] op_sel_hi:[1,0,1]
	v_pk_fma_f32 v[26:27], v[34:35], s[16:17], v[26:27] op_sel_hi:[1,0,1]
	v_pk_fma_f32 v[24:25], v[50:51], s[16:17], v[24:25] op_sel_hi:[1,0,1]
	v_pk_fma_f32 v[22:23], v[36:37], s[16:17], v[22:23] op_sel_hi:[1,0,1]
	v_pk_fma_f32 v[20:21], v[52:53], s[16:17], v[20:21] op_sel_hi:[1,0,1]
	v_pk_fma_f32 v[32:33], v[38:39], s[16:17], v[18:19] op_sel_hi:[1,0,1]
	v_pk_fma_f32 v[34:35], v[54:55], s[16:17], v[16:17] op_sel_hi:[1,0,1]
	v_cvt_pk_bf16_f32 v16, v28, v29
	v_cvt_pk_bf16_f32 v17, v30, v31
	v_cvt_pk_bf16_f32 v18, v24, v25
	v_cvt_pk_bf16_f32 v19, v26, v27
	v_cvt_pk_bf16_f32 v20, v20, v21
	v_cvt_pk_bf16_f32 v21, v22, v23
	v_cvt_pk_bf16_f32 v22, v34, v35
	v_cvt_pk_bf16_f32 v23, v32, v33
	global_store_dwordx4 v[44:45], v[16:19], off
	global_store_dwordx4 v[40:41], v[20:23], off
	v_lshl_add_u64 v[24:25], v[132:133], 0, s[52:53]
	s_nop 0
	v_lshl_add_u64 v[20:21], s[10:11], 0, v[24:25]
	s_nop 0
	v_lshl_add_u64 v[26:27], s[12:13], 0, v[42:43]
	v_lshl_add_u64 v[24:25], s[12:13], 0, v[24:25]
	s_nop 0
	s_waitcnt vmcnt(15)
	v_lshlrev_b32_e32 v28, 16, v192
	v_and_b32_e32 v29, 0xffff0000, v192
	v_lshlrev_b32_e32 v16, 16, v193
	v_and_b32_e32 v17, 0xffff0000, v193
	v_lshlrev_b32_e32 v30, 16, v194
	v_and_b32_e32 v31, 0xffff0000, v194
	v_lshlrev_b32_e32 v18, 16, v195
	v_and_b32_e32 v19, 0xffff0000, v195
	s_nop 0
	s_waitcnt vmcnt(14)
	v_lshlrev_b32_e32 v32, 16, v188
	v_and_b32_e32 v33, 0xffff0000, v188
	v_lshlrev_b32_e32 v20, 16, v189
	v_and_b32_e32 v21, 0xffff0000, v189
	v_lshlrev_b32_e32 v34, 16, v190
	v_and_b32_e32 v35, 0xffff0000, v190
	v_lshlrev_b32_e32 v22, 16, v191
	v_and_b32_e32 v23, 0xffff0000, v191
	v_pk_fma_f32 v[14:15], v[16:17], s[16:17], v[14:15] op_sel_hi:[1,0,1]
	v_pk_fma_f32 v[12:13], v[28:29], s[16:17], v[12:13] op_sel_hi:[1,0,1]
	v_pk_fma_f32 v[10:11], v[18:19], s[16:17], v[10:11] op_sel_hi:[1,0,1]
	v_pk_fma_f32 v[8:9], v[30:31], s[16:17], v[8:9] op_sel_hi:[1,0,1]
	v_pk_fma_f32 v[6:7], v[20:21], s[16:17], v[6:7] op_sel_hi:[1,0,1]
	v_pk_fma_f32 v[4:5], v[32:33], s[16:17], v[4:5] op_sel_hi:[1,0,1]
	v_pk_fma_f32 v[16:17], v[22:23], s[16:17], v[2:3] op_sel_hi:[1,0,1]
	v_pk_fma_f32 v[18:19], v[34:35], s[16:17], v[0:1] op_sel_hi:[1,0,1]
	v_cvt_pk_bf16_f32 v0, v12, v13
	v_cvt_pk_bf16_f32 v1, v14, v15
	v_cvt_pk_bf16_f32 v2, v8, v9
	v_cvt_pk_bf16_f32 v3, v10, v11
	v_cvt_pk_bf16_f32 v4, v4, v5
	v_cvt_pk_bf16_f32 v5, v6, v7
	v_cvt_pk_bf16_f32 v6, v18, v19
	v_cvt_pk_bf16_f32 v7, v16, v17
	global_store_dwordx4 v[26:27], v[0:3], off
	global_store_dwordx4 v[24:25], v[4:7], off
	s_cbranch_vccnz .LBB0_561
	s_andn2_b64 vcc, exec, s[8:9]
	s_cbranch_vccnz .LBB0_560
	s_barrier
	s_branch .LBB0_560
